# MLA: 4-slot LDS ring with a DMA lead of three stages; the even tile's first K fragments are prefetched from LDS in the odd tile's PV/exp gaps in front of the stage barrier (side-job tile moved to 0x18
# speedup vs baseline: 1.0144x; 1.0144x over previous
; #define LAS __attribute__((address_space(3)))
; #define WAITV(n) asm volatile("s_waitcnt vmcnt(%0)" ::"n"(n) : "memory")
; #define SBAR() do { asm volatile("s_waitcnt lgkmcnt(0)" ::: "memory"); __builtin_amdgcn_s_barrier(); asm volatile("" ::: "memory"); } while (0)
; DEV int otid() { int t = threadIdx.x; asm volatile("" : "+v"(t)); return t; }
; DEV unsigned char* ows_(unsigned char* w) { gptr_t g = (gptr_t)w; asm volatile("" : "+s"(g)); return (unsigned char*)g; }
; DEV unsigned lds_addr(LAS char* p) { return (unsigned)(uintptr_t)p; }
; DEV void sj_tick(const Params& p, int layer, SideJob& sj, LAS char* lds, int tid) {
;     LAS float* tile = (LAS float*)(lds + SJ_TILE_OFF);
; template <int VAR> DEV void mla_unit(const Params& p, int layer, int b, int hd, int tokbase, int t0, int t1, LAS char* lds, SideJob& sj) {
;     unsigned char* ws = ows_(p.ws); const int tid = otid(), lane = tid & 63, wid = tid >> 6, r = lane & 31, h = lane >> 5;
;     constexpr int STG = MLA_IMG;
;     const float cinit = 15.0f - ((const float*)(ws + WS_SCAL))[layer * 8 + 1];
;     const int tok = tokbase + 32 * wid + r;
;     v8i qf[2];
; #pragma unroll
;     for (int sx = 0; sx < 2; ++sx) { const u32x4* q8 = (const u32x4*)(ws + WS_QC + (size_t)tok * 768 + hd * 128 + 64 * sx + 32 * h); const u32x4 a = q8[0], bq = q8[1];
;         qf[sx] = (v8i){(int)a[0], (int)a[1], (int)a[2], (int)a[3], (int)bq[0], (int)bq[1], (int)bq[2], (int)bq[3]}; }
;     const unsigned char* imgs = ws + WS_KVC + (size_t)((b * 6 + hd) * 130) * MLA_IMG;
;     const unsigned ldsw = (unsigned)__builtin_amdgcn_readfirstlane((int)(lds_addr(lds) + (unsigned)(wid * (STG / 8))));
;     ...
;     f32x16 cini, sA0, sA1, sB0, sB1, o0, o1, lacc;
; #pragma unroll
;     for (int i = 0; i < 16; ++i) { cini[i] = cinit; o0[i] = 0.f; o1[i] = 0.f; lacc[i] = 0.f; }
;     const unsigned koffl = (unsigned)(2 * h * 1024 + r * 16);
;     const unsigned voffl = (unsigned)MLA_VOFF + (unsigned)(2 * h * 1024 + r * 16);
;     const int ns = t1 - t0;
;     MLA_ISSUE(t0, 0);
;     WAITV(0); SBAR();
;     if (ns > 1) MLA_ISSUE(t0 + 1, 1);
;     { LAS char* kp = lds + koffl;
;       sA0 = MFMA8(mla_kf8(kp, 0, 0), qf[0], cini); sA1 = MFMA8(mla_kf8(kp, 1, 0), qf[0], cini);
;       sA0 = MFMA8(mla_kf8(kp, 0, 1), qf[1], sA0); sA1 = MFMA8(mla_kf8(kp, 1, 1), qf[1], sA1);
.LBB0_758:
	s_mov_b64 s[8:9], 0
	s_and_b64 vcc, exec, s[6:7]
	s_cbranch_vccz .LBB0_765
	s_cmpk_gt_i32 s64, 0x2ff
	s_mov_b64 s[6:7], -1
	s_cbranch_scc0 .LBB0_808
	s_add_i32 s2, s64, 0xfffffd00
	s_mul_hi_u32 s3, s2, 0xaaaaaaab
	s_lshr_b32 s3, s3, 2
	s_mul_i32 s6, s3, 6
	s_sub_i32 s30, s2, s6
	s_lshl_b32 s3, s3, 8
	s_mov_b64 s[6:7], s[38:39]
	v_mov_b32_e32 v6, v246
	s_add_i32 s3, s3, 0x8000
	s_lshl_b64 s[8:9], s[48:49], 2
	v_and_b32_e32 v9, 31, v6
	v_ashrrev_i32_e32 v7, 6, v6
	v_or_b32_e32 v2, s3, v9
	s_add_u32 s8, s6, s8
	v_lshl_add_u32 v138, v7, 5, v2
	v_mov_b64_e32 v[2:3], s[6:7]
	s_movk_i32 s3, 0x300
	s_addc_u32 s9, s7, s9
	v_mad_i64_i32 v[2:3], s[20:21], v138, s3, v[2:3]
	s_lshl_b32 s30, s30, 7
	v_lshl_add_u64 v[2:3], v[2:3], 0, s[30:31]
	v_and_b32_e32 v178, 32, v6
	v_lshl_add_u64 v[2:3], v[2:3], 0, v[178:179]
	s_mov_b64 s[20:21], 0x33370100
	s_mov_b32 s3, 0x33370000
	v_lshl_add_u64 v[4:5], v[2:3], 0, s[20:21]
	v_add_co_u32_e32 v2, vcc, s3, v2
	s_mul_i32 s3, s2, 0x82
	s_nop 0
	v_addc_co_u32_e32 v3, vcc, 0, v3, vcc
	global_load_dwordx4 v[122:125], v[2:3], off offset:256
	global_load_dword v8, v247, s[8:9] offset:4
	global_load_dwordx4 v[126:129], v[4:5], off offset:16
	global_load_dwordx4 v[118:121], v[4:5], off offset:80
	global_load_dwordx4 v[114:117], v[4:5], off offset:64
	s_mul_i32 s2, s2, 0x30c000
	s_movk_i32 s8, 0xc00
	s_mul_hi_u32 s3, s3, 0x6000
	v_mul_lo_u32 v2, v7, s8
	v_bfe_u32 v140, v6, 5, 1
	s_add_u32 s8, s6, s2
	v_lshlrev_b32_e32 v3, 4, v9
	v_and_b32_e32 v4, 63, v6
	s_addc_u32 s9, s7, s3
	v_lshl_or_b32 v7, v140, 11, v3
	v_ashrrev_i32_e32 v3, 31, v2
	v_readfirstlane_b32 s20, v2
	v_lshlrev_b32_e32 v178, 4, v4
	v_lshl_add_u64 v[2:3], s[8:9], 0, v[2:3]
	v_lshl_add_u64 v[2:3], v[2:3], 0, v[178:179]
	s_mov_b64 s[8:9], 0x35b00100
	s_add_i32 s2, s20, 0
	v_lshl_add_u64 v[4:5], v[2:3], 0, s[8:9]
	s_mov_b32 s3, m0
	s_mov_b32 m0, s2
	s_nop 0
	global_load_lds_dwordx4 v[4:5], off
	s_mov_b32 m0, s3
	s_mov_b64 s[8:9], 0x35b00500
	v_lshl_add_u64 v[4:5], v[2:3], 0, s[8:9]
	s_add_i32 s3, s2, 0x400
	s_mov_b32 s8, m0
	s_mov_b32 m0, s3
	s_nop 0
	global_load_lds_dwordx4 v[4:5], off
	s_mov_b32 m0, s8
	s_mov_b64 s[8:9], 0x35b00900
	v_lshl_add_u64 v[4:5], v[2:3], 0, s[8:9]
	s_add_i32 s3, s2, 0x800
	s_mov_b32 s8, m0
	s_mov_b32 m0, s3
	s_nop 0
	global_load_lds_dwordx4 v[4:5], off
	s_mov_b32 m0, s8
	s_waitcnt vmcnt(0)
	s_waitcnt lgkmcnt(0)
	s_barrier
	s_mov_b64 s[8:9], 0x35b06100
	v_lshl_add_u64 v[4:5], v[2:3], 0, s[8:9]
	s_add_i32 s3, s2, 0x6000
	s_mov_b32 s8, m0
	s_mov_b32 m0, s3
	s_nop 0
	global_load_lds_dwordx4 v[4:5], off
	s_mov_b32 m0, s8
	s_mov_b64 s[8:9], 0x35b06500
	v_lshl_add_u64 v[4:5], v[2:3], 0, s[8:9]
	s_add_i32 s3, s2, 0x6400
	s_mov_b32 s8, m0
	s_mov_b32 m0, s3
	s_nop 0
	global_load_lds_dwordx4 v[4:5], off
	s_mov_b32 m0, s8
	s_mov_b64 s[8:9], 0x35b06900
	v_lshl_add_u64 v[2:3], v[2:3], 0, s[8:9]
	s_addk_i32 s2, 0x6800
	s_mov_b32 s3, m0
	s_mov_b32 m0, s2
	s_nop 0
	global_load_lds_dwordx4 v[2:3], off
	s_mov_b32 m0, s3
	v_add_u32_e32 v141, 0, v7
	ds_read_b128 v[18:21], v141
	ds_read_b128 v[34:37], v141 offset:512
	ds_read_b128 v[22:25], v141 offset:1024
	ds_read_b128 v[38:41], v141 offset:1536
	ds_read_b128 v[58:61], v141 offset:4096
	ds_read_b128 v[50:53], v141 offset:4608
	ds_read_b128 v[62:65], v141 offset:5120
	ds_read_b128 v[54:57], v141 offset:5632
	v_ashrrev_i32_e32 v76, 4, v6
	s_movk_i32 s2, 0x104
	v_mul_lo_u32 v3, v76, s2
	s_add_i32 s2, 0, 0x18000
	s_and_b32 s37, s29, 3
	v_lshlrev_b32_e32 v2, 2, v6
	s_cmp_gt_i32 s33, 63
	v_and_b32_e32 v2, 60, v2
	s_cselect_b64 s[8:9], -1, 0
	s_cmp_eq_u32 s37, 3
	v_lshlrev_b32_e32 v74, 2, v2
	v_cmp_lt_u32_e64 s[40:41], 31, v2
	v_lshlrev_b32_e32 v2, 3, v6
	s_cselect_b64 s[20:21], -1, 0
	v_ashrrev_i32_e32 v78, 3, v6
	v_and_b32_e32 v178, 56, v2
	s_or_b64 s[8:9], s[8:9], s[20:21]
	s_waitcnt vmcnt(0)
	v_mov_b64_e32 v[192:193], v[188:189]
	v_mov_b64_e32 v[196:197], v[184:185]
	v_add3_u32 v77, s2, v3, v74
	v_lshl_add_u32 v79, v78, 2, s2
	v_mul_u32_u24_e32 v80, 0x104, v178
	s_and_b64 vcc, exec, s[8:9]
	v_mov_b64_e32 v[190:191], v[186:187]
	v_mov_b64_e32 v[194:195], v[182:183]
	s_mov_b32 s62, s36
	s_mov_b32 s63, s33
	s_cbranch_vccnz .LBB0_783
	s_add_i32 s20, s33, s12
	s_cmpk_lt_i32 s36, 0x100
	s_cselect_b64 s[50:51], -1, 0
	s_lshl_b32 s55, s36, 6
	s_cmpk_gt_i32 s36, 0xff
	s_mov_b64 s[58:59], -1
	s_cbranch_scc1 .LBB0_763
	s_ashr_i32 s21, s20, 31
	s_lshl_b64 s[52:53], s[20:21], 21
	s_add_u32 s8, s44, s52
	s_addc_u32 s9, s45, s53
	s_add_u32 s52, s46, s52
	s_addc_u32 s53, s47, s53
	s_lshl_b64 s[56:57], s[20:21], 20
	s_add_u32 s56, s13, s56
	s_addc_u32 s57, s16, s57
	s_and_b32 s54, s55, 0x3c0
	s_ashr_i32 s65, s36, 4
	s_mov_b64 s[58:59], 0

; #define WAITV(n) asm volatile("s_waitcnt vmcnt(%0)" ::"n"(n) : "memory")
; #define SBAR() do { asm volatile("s_waitcnt lgkmcnt(0)" ::: "memory"); __builtin_amdgcn_s_barrier(); asm volatile("" ::: "memory"); } while (0)
; DEV int otid() { int t = threadIdx.x; asm volatile("" : "+v"(t)); return t; }
; DEV unsigned char* ows_(unsigned char* w) { gptr_t g = (gptr_t)w; asm volatile("" : "+s"(g)); return (unsigned char*)g; }
; DEV unsigned lds_addr(LAS char* p) { return (unsigned)(uintptr_t)p; }
; #define MLA_ISSUE(t_, st_) do { const unsigned char* s_ = imgs + (size_t)(t_) * MLA_IMG + wid * (STG / 8) + lane * 16; const unsigned d_ = ldsw + (unsigned)((st_) * STG); \
;     _Pragma("unroll") for (int i_ = 0; i_ < STG / 8192; ++i_) glds16a(s_ + i_ * 1024, d_ + i_ * 1024); } while (0)
; template <int VAR> DEV void mla_unit(const Params& p, int layer, int b, int hd, int tokbase, int t0, int t1, LAS char* lds, SideJob& sj) {
;     unsigned char* ws = ows_(p.ws); const int tid = otid(), lane = tid & 63, wid = tid >> 6, r = lane & 31, h = lane >> 5;
;     constexpr int STG = MLA_IMG;
;     const float cinit = 15.0f - ((const float*)(ws + WS_SCAL))[layer * 8 + 1];
;     const int tok = tokbase + 32 * wid + r;
;     v8i qf[2];
; #pragma unroll
;     for (int sx = 0; sx < 2; ++sx) { const u32x4* q8 = (const u32x4*)(ws + WS_QC + (size_t)tok * 768 + hd * 128 + 64 * sx + 32 * h); const u32x4 a = q8[0], bq = q8[1];
;         qf[sx] = (v8i){(int)a[0], (int)a[1], (int)a[2], (int)a[3], (int)bq[0], (int)bq[1], (int)bq[2], (int)bq[3]}; }
;     const unsigned char* imgs = ws + WS_KVC + (size_t)((b * 6 + hd) * 130) * MLA_IMG;
;     const unsigned ldsw = (unsigned)__builtin_amdgcn_readfirstlane((int)(lds_addr(lds) + (unsigned)(wid * (STG / 8))));
;     ...
;     f32x16 cini, sA0, sA1, sB0, sB1, o0, o1, lacc;
; #pragma unroll
;     for (int i = 0; i < 16; ++i) { cini[i] = cinit; o0[i] = 0.f; o1[i] = 0.f; lacc[i] = 0.f; }
;     const unsigned koffl = (unsigned)(2 * h * 1024 + r * 16);
;     const unsigned voffl = (unsigned)MLA_VOFF + (unsigned)(2 * h * 1024 + r * 16);
;     const int ns = t1 - t0;
;     MLA_ISSUE(t0, 0);
;     WAITV(0); SBAR();
.LBB0_808:
	s_and_b64 vcc, exec, s[6:7]
	s_cbranch_vccz .LBB0_749
	s_ashr_i32 s2, s64, 6
	s_mul_hi_i32 s3, s2, 0x2aaaaaab
	s_lshr_b32 s6, s3, 31
	s_add_i32 s3, s3, s6
	s_mul_i32 s6, s3, 6
	s_sub_i32 s37, s2, s6
	s_lshl_b32 s6, s64, 8
	s_lshl_b32 s3, s3, 14
	s_and_b32 s6, s6, 0x3f00
	s_or_b32 s3, s3, s6
	s_mov_b64 s[6:7], s[38:39]
	v_mov_b32_e32 v52, v246
	s_lshl_b64 s[8:9], s[48:49], 2
	v_and_b32_e32 v7, 31, v52
	v_ashrrev_i32_e32 v6, 6, v52
	s_add_u32 s8, s6, s8
	v_or_b32_e32 v2, s3, v7
	s_addc_u32 s9, s7, s9
	v_lshl_add_u32 v180, v6, 5, v2
	v_mov_b64_e32 v[2:3], s[6:7]
	s_movk_i32 s3, 0x300
	global_load_dword v8, v247, s[8:9] offset:4
	v_mad_i64_i32 v[2:3], s[8:9], v180, s3, v[2:3]
	s_lshl_b32 s8, s37, 7
	s_ashr_i32 s9, s8, 31
	v_lshl_add_u64 v[2:3], v[2:3], 0, s[8:9]
	v_and_b32_e32 v178, 32, v52
	v_lshl_add_u64 v[2:3], v[2:3], 0, v[178:179]
	s_mov_b64 s[8:9], 0x33370100
	s_mov_b32 s3, 0x33370000
	v_lshl_add_u64 v[4:5], v[2:3], 0, s[8:9]
	v_add_co_u32_e32 v2, vcc, s3, v2
	s_mul_i32 s3, s2, 0x82
	s_nop 0
	v_addc_co_u32_e32 v3, vcc, 0, v3, vcc
	global_load_dwordx4 v[138:141], v[2:3], off offset:256
	global_load_dwordx4 v[142:145], v[4:5], off offset:16
	global_load_dwordx4 v[134:137], v[4:5], off offset:80
	global_load_dwordx4 v[130:133], v[4:5], off offset:64
	s_mul_i32 s8, s2, 0x30c000
	s_movk_i32 s2, 0xc00
	s_mul_hi_i32 s9, s3, 0x6000
	v_mul_lo_u32 v50, v6, s2
	s_add_u32 s20, s6, s8
	v_and_b32_e32 v3, 63, v52
	v_bfe_u32 v198, v52, 5, 1
	s_addc_u32 s21, s7, s9
	v_lshlrev_b32_e32 v4, 4, v7
	v_ashrrev_i32_e32 v51, 31, v50
	v_lshl_or_b32 v199, v198, 11, v4
	v_lshl_add_u64 v[4:5], s[20:21], 0, v[50:51]
	v_lshlrev_b32_e32 v178, 4, v3
	v_readfirstlane_b32 s60, v50
	v_lshl_add_u64 v[18:19], v[4:5], 0, v[178:179]
	s_mov_b64 s[20:21], 0x35800100
	s_add_i32 s60, s60, 0
	v_lshl_add_u64 v[4:5], v[18:19], 0, s[20:21]
	s_mov_b32 s2, m0
	s_mov_b32 m0, s60
	s_nop 0
	global_load_lds_dwordx4 v[4:5], off
	s_mov_b32 m0, s2
	s_mov_b64 s[20:21], 0x35800500
	v_lshl_add_u64 v[4:5], v[18:19], 0, s[20:21]
	s_add_i32 s2, s60, 0x400
	s_mov_b32 s3, m0
	s_mov_b32 m0, s2
	s_nop 0
	global_load_lds_dwordx4 v[4:5], off
	s_mov_b32 m0, s3
	s_mov_b64 s[20:21], 0x35800900
	v_lshl_add_u64 v[4:5], v[18:19], 0, s[20:21]
	s_add_i32 s2, s60, 0x800
	s_mov_b32 s3, m0
	s_mov_b32 m0, s2
	s_nop 0
	global_load_lds_dwordx4 v[4:5], off
	s_mov_b32 m0, s3
	s_waitcnt vmcnt(0)
	s_waitcnt lgkmcnt(0)
	s_barrier
; #define LAS __attribute__((address_space(3)))
; #define WAITV(n) asm volatile("s_waitcnt vmcnt(%0)" ::"n"(n) : "memory")
; #define SBAR() do { asm volatile("s_waitcnt lgkmcnt(0)" ::: "memory"); __builtin_amdgcn_s_barrier(); asm volatile("" ::: "memory"); } while (0)
; DEV float ex2(float x) { return __builtin_amdgcn_exp2f(x); }
; #define MFMA8(a, b, c) __builtin_amdgcn_mfma_scale_f32_32x32x64_f8f6f4((a), (b), (c), 0, 0, 0, 0x7f7f7f7f, 0, 0x7c7c7c7c)
; #define MLA_ISSUE(t_, st_) do { const unsigned char* s_ = imgs + (size_t)(t_) * MLA_IMG + wid * (STG / 8) + lane * 16; const unsigned d_ = ldsw + (unsigned)((st_) * STG); \
;     _Pragma("unroll") for (int i_ = 0; i_ < STG / 8192; ++i_) glds16a(s_ + i_ * 1024, d_ + i_ * 1024); } while (0)
; template <int VAR> DEV void mla_unit(const Params& p, int layer, int b, int hd, int tokbase, int t0, int t1, LAS char* lds, SideJob& sj) {
;     ...
;     f32x16 cini, sA0, sA1, sB0, sB1, o0, o1, lacc;
; #pragma unroll
;     for (int i = 0; i < 16; ++i) { cini[i] = cinit; o0[i] = 0.f; o1[i] = 0.f; lacc[i] = 0.f; }
;     const unsigned koffl = (unsigned)(2 * h * 1024 + r * 16);
;     const unsigned voffl = (unsigned)MLA_VOFF + (unsigned)(2 * h * 1024 + r * 16);
;     const int ns = t1 - t0;
;     MLA_ISSUE(t0, 0);
;     WAITV(0); SBAR();
;     if (ns > 1) MLA_ISSUE(t0 + 1, 1);
;     { LAS char* kp = lds + koffl;
;       sA0 = MFMA8(mla_kf8(kp, 0, 0), qf[0], cini); sA1 = MFMA8(mla_kf8(kp, 1, 0), qf[0], cini);
;       sA0 = MFMA8(mla_kf8(kp, 0, 1), qf[1], sA0); sA1 = MFMA8(mla_kf8(kp, 1, 1), qf[1], sA1);
; #pragma unroll
;       for (int i = 0; i < 16; ++i) { sA0[i] = ex2(sA0[i]); sA1[i] = ex2(sA1[i]); } }
	s_mov_b64 s[20:21], 0x35806100
	v_lshl_add_u64 v[20:21], v[18:19], 0, s[20:21]
	s_add_i32 s2, s60, 0x6000
	s_mov_b32 s3, m0
	s_mov_b32 m0, s2
	s_nop 0
	global_load_lds_dwordx4 v[20:21], off
	s_mov_b32 m0, s3
	s_mov_b64 s[20:21], 0x35806500
	v_lshl_add_u64 v[20:21], v[18:19], 0, s[20:21]
	s_add_i32 s2, s60, 0x6400
	s_mov_b32 s3, m0
	s_mov_b32 m0, s2
	s_nop 0
	global_load_lds_dwordx4 v[20:21], off
	s_mov_b32 m0, s3
	s_mov_b64 s[20:21], 0x35806900
	v_lshl_add_u64 v[18:19], v[18:19], 0, s[20:21]
	s_add_i32 s2, s60, 0x6800
	s_mov_b32 s3, m0
	s_mov_b32 m0, s2
	s_nop 0
	global_load_lds_dwordx4 v[18:19], off
	s_mov_b32 m0, s3
	v_add_u32_e32 v200, 0, v199
	ds_read_b128 v[18:21], v200
	ds_read_b128 v[22:25], v200 offset:1024
	s_waitcnt vmcnt(3)
	v_ashrrev_i32_e32 v191, 4, v52
	s_movk_i32 s2, 0x104
	v_ashrrev_i32_e32 v195, 3, v52
	v_ashrrev_i32_e32 v181, 31, v180
	s_mov_b32 s62, 0
	v_mov_b32_e32 v193, v179
	v_mov_b32_e32 v146, 0
	v_mov_b32_e32 v147, 0
	v_mov_b32_e32 v148, 0
	v_mov_b32_e32 v149, 0
	v_mov_b32_e32 v150, 0
	v_mov_b32_e32 v151, 0
	v_mov_b32_e32 v152, 0
	v_mov_b32_e32 v153, 0
	s_mov_b32 s61, 0
	v_sub_f32_e32 v2, 0x41700000, v8
	v_mov_b32_e32 v3, v2
	v_mov_b32_e32 v4, v2
	v_mov_b32_e32 v5, v2
	v_mov_b32_e32 v6, v2
	v_mov_b32_e32 v7, v2
	v_mov_b32_e32 v8, v2
	v_mov_b32_e32 v9, v2
	v_mov_b32_e32 v10, v2
	v_mov_b32_e32 v11, v2
	v_mov_b32_e32 v12, v2
	v_mov_b32_e32 v13, v2
	v_mov_b32_e32 v14, v2
	v_mov_b32_e32 v15, v2
	v_mov_b32_e32 v16, v2
	v_mov_b32_e32 v17, v2
	s_waitcnt lgkmcnt(0)
	s_nop 0
	v_mfma_scale_f32_32x32x64_f8f6f4 v[18:33], v[18:25], v[138:145], v[2:17], v209, v208 op_sel_hi:[0,0,0]
	ds_read_b128 v[34:37], v200 offset:512
	ds_read_b128 v[38:41], v200 offset:1536
	s_waitcnt lgkmcnt(0)
	v_mfma_scale_f32_32x32x64_f8f6f4 v[34:49], v[34:41], v[138:145], v[2:17], v209, v208 op_sel_hi:[0,0,0]
	ds_read_b128 v[54:57], v200 offset:4096
	ds_read_b128 v[58:61], v200 offset:5120
	s_waitcnt lgkmcnt(0)
	v_mfma_scale_f32_32x32x64_f8f6f4 v[18:33], v[54:61], v[130:137], v[18:33], v209, v208 op_sel_hi:[0,0,0]
	ds_read_b128 v[54:57], v200 offset:4608
	ds_read_b128 v[58:61], v200 offset:5632
	s_waitcnt lgkmcnt(0)
	v_mfma_scale_f32_32x32x64_f8f6f4 v[34:49], v[54:61], v[130:137], v[34:49], v209, v208 op_sel_hi:[0,0,0]
	s_nop 15
	v_exp_f32_e32 v82, v18
	v_lshlrev_b32_e32 v18, 2, v52
	v_and_b32_e32 v190, 60, v18
	v_exp_f32_e32 v83, v19
	v_mul_lo_u32 v18, v191, s2
	s_add_i32 s2, 0, 0x18000
	v_lshlrev_b32_e32 v19, 2, v190
	v_add3_u32 v194, s2, v18, v19
	v_lshlrev_b32_e32 v18, 3, v52
	v_exp_f32_e32 v84, v20
	v_exp_f32_e32 v85, v21
	v_exp_f32_e32 v86, v22
	v_exp_f32_e32 v87, v23
	v_exp_f32_e32 v88, v24
	v_exp_f32_e32 v89, v25
	v_exp_f32_e32 v66, v34
	v_exp_f32_e32 v67, v35
	v_exp_f32_e32 v68, v36
	v_mov_b32_e32 v69, v37
	v_mov_b32_e32 v70, v38
	v_mov_b32_e32 v71, v39
	v_mov_b32_e32 v72, v40
	v_mov_b32_e32 v73, v41
	v_mov_b32_e32 v74, v42
	v_mov_b32_e32 v75, v43
	v_mov_b32_e32 v76, v44
	v_mov_b32_e32 v77, v45
	v_mov_b32_e32 v78, v46
	v_mov_b32_e32 v79, v47
	v_mov_b32_e32 v80, v48
	v_mov_b32_e32 v81, v49
	v_exp_f32_e32 v90, v26
	v_exp_f32_e32 v91, v27
	v_exp_f32_e32 v92, v28
	v_exp_f32_e32 v93, v29
	v_exp_f32_e32 v94, v30
	v_exp_f32_e32 v95, v31
	v_exp_f32_e32 v96, v32
	v_exp_f32_e32 v97, v33
	v_and_b32_e32 v192, 56, v18
	v_or_b32_e32 v18, s8, v178
	v_mov_b32_e32 v19, s9
	v_lshl_add_u64 v[18:19], v[18:19], 0, v[50:51]
	v_lshl_add_u64 v[18:19], s[6:7], 0, v[18:19]
	s_mov_b64 s[8:9], 0x3580c100
	v_mov_b32_e32 v34, 0
	v_cmp_lt_u32_e64 s[40:41], 31, v190
	v_lshl_add_u32 v196, v195, 2, s2
	v_mul_u32_u24_e32 v197, 0x104, v192
	v_lshl_add_u64 v[162:163], v[18:19], 0, s[8:9]
	s_add_i32 s2, s60, 0xc000
	s_mov_b32 s3, m0
	s_mov_b32 m0, s2
	s_nop 0
	global_load_lds_dwordx4 v[162:163], off
	global_load_lds_dwordx4 v[162:163], off offset:1024
	global_load_lds_dwordx4 v[162:163], off offset:2048
	s_mov_b32 m0, s3
	s_mov_b64 s[8:9], 0x6000
	v_lshl_add_u64 v[162:163], v[162:163], 0, s[8:9]
	v_mov_b32_e32 v35, v34
	v_mov_b32_e32 v36, v34
	v_mov_b32_e32 v37, v34
	v_mov_b32_e32 v38, v34
	v_mov_b32_e32 v39, v34
	v_mov_b32_e32 v40, v34
	v_mov_b32_e32 v41, v34
	v_mov_b32_e32 v42, v34
	v_mov_b32_e32 v43, v34
	v_mov_b32_e32 v44, v34
	v_mov_b32_e32 v45, v34
	v_mov_b32_e32 v46, v34
	v_mov_b32_e32 v47, v34
	v_mov_b32_e32 v48, v34
	v_mov_b32_e32 v49, v34
	v_mov_b32_e32 v18, v34
	v_mov_b32_e32 v19, v34
	v_mov_b32_e32 v20, v34
	v_mov_b32_e32 v21, v34
	v_mov_b32_e32 v22, v34
	v_mov_b32_e32 v23, v34
	v_mov_b32_e32 v24, v34
	v_mov_b32_e32 v25, v34
	v_mov_b32_e32 v26, v34
	v_mov_b32_e32 v27, v34
	v_mov_b32_e32 v28, v34
	v_mov_b32_e32 v29, v34
	v_mov_b32_e32 v30, v34
	v_mov_b32_e32 v31, v34
	v_mov_b32_e32 v32, v34
	v_mov_b32_e32 v33, v34
	v_mov_b32_e32 v50, v34
	v_mov_b32_e32 v51, v34
	v_mov_b32_e32 v52, v34
	v_mov_b32_e32 v53, v34
	v_mov_b32_e32 v54, v34
	v_mov_b32_e32 v55, v34
	v_mov_b32_e32 v56, v34
	v_mov_b32_e32 v57, v34
	v_mov_b32_e32 v58, v34
	v_mov_b32_e32 v59, v34
	v_mov_b32_e32 v60, v34
	v_mov_b32_e32 v61, v34
	v_mov_b32_e32 v62, v34
	v_mov_b32_e32 v63, v34
	v_mov_b32_e32 v64, v34
	v_mov_b32_e32 v65, v34
	s_waitcnt vmcnt(3)
	s_waitcnt lgkmcnt(0)
	s_barrier
	v_mov_b64_e32 v[210:211], s[76:77]
	v_mov_b64_e32 v[212:213], s[78:79]
	v_mov_b64_e32 v[214:215], s[80:81]
	v_mov_b64_e32 v[216:217], s[82:83]
	s_cmp_ge_u32 s60, 0x3000
	s_cbranch_scc0 .Lmla_prio_skip
	s_setprio 1

; #define LAS __attribute__((address_space(3)))
; #define WAITV(n) asm volatile("s_waitcnt vmcnt(%0)" ::"n"(n) : "memory")
; template <int VAR> DEV void mla_step(f32x16& C0, f32x16& C1, f32x16& P0, f32x16& P1, f32x16& o0, f32x16& o1, f32x16& lacc,
;                   const v8i (&qf)[2], const f32x16& cini, LAS char* kp, LAS char* vp, v8i& pw) {
;     v8i kf[2], vf[2];
;     const v8i ones8 = {0x38383838, 0x38383838, 0x38383838, 0x38383838, 0x38383838, 0x38383838, 0x38383838, 0x38383838};
;     kf[0] = mla_kf8(kp, 0, 0); kf[1] = mla_kf8(kp, 1, 0);
;     MLA_SB();
; #pragma unroll
;     for (int g = 0; g < 4; ++g) {
;         const int kb = g & 1, sx = g >> 1;
;         if (kb) C1 = MFMA8(kf[1], qf[sx], sx == 0 ? cini : C1); else C0 = MFMA8(kf[0], qf[sx], sx == 0 ? cini : C0);
;         if (g < 2) kf[kb] = mla_kf8(kp, kb, 1);
;         if (g >= 2) vf[g - 2] = mla_vf8(vp, g - 2);
; #pragma unroll
;         for (int j = 0; j < 2; ++j) { const int w = 2 * g + j, e = 4 * w;
;             if (VAR == 3) pw[w] = __builtin_bit_cast(int, (e < 16) ? P0[e] : P1[e - 16]);
;             else pw[w] = (int)((e < 16) ? pk_bf8x4(P0[e], P0[e + 1], P0[e + 2], P0[e + 3], pw[w]) : pk_bf8x4(P1[e - 16], P1[e - 15], P1[e - 14], P1[e - 13], pw[w])); }
;         if (g == 3) MLA_PIN(pw);
;         MLA_SB();
;     }
; #pragma unroll
;     for (int g = 0; g < 3; ++g) {
;         if (g == 0) o0 = MFMA8PV(vf[0], pw, o0); else if (g == 1) o1 = MFMA8PV(vf[1], pw, o1); else lacc = MFMA8PV(ones8, pw, lacc);
;         const int e0 = (g * 32) / 3, e1 = ((g + 1) * 32) / 3;
; #pragma unroll
;         for (int e = e0; e < e1; ++e) { if (VAR == 2 || VAR == 3) continue; if (e < 16) C0[e] = ex2(C0[e]); else C1[e - 16] = ex2(C1[e - 16]); }
;         if (g < 2) MLA_PIN(C0);
;         if (g > 0) MLA_PIN(C1);
;         MLA_SB();
;     }
; }
; template <int VAR> DEV void mla_unit(const Params& p, int layer, int b, int hd, int tokbase, int t0, int t1, LAS char* lds, SideJob& sj) {
;     ...
;     for (int s = 0; s < ns; ++s) {
;         sj_tick(p, layer, sj, lds, tid);
;         { LAS char* base = lds + slot * STG; mla_step<VAR>(sB0, sB1, sA0, sA1, o0, o1, lacc, qf, cini, base + MLA_KSUB + koffl, base + voffl, pw); }
;         if (s + 1 < ns) {
;             const int nslot = (slot == 2) ? 0 : slot + 1;
;             WAITV(0); SBAR();
;             if (s + 2 < ns) MLA_ISSUE(t0 + s + 2, (nslot == 2) ? 0 : nslot + 1);
.LBB0_812:
	s_mul_i32 s2, s62, 0x6000
	v_add_u32_e32 v172, s2, v200
	s_add_i32 s3, s62, 1
	s_and_b32 s3, s3, 3
	s_mul_i32 s3, s3, 0x6000
	ds_read_b128 v[98:101], v172 offset:8192
	ds_read_b128 v[106:109], v172 offset:8704
	ds_read_b128 v[102:105], v172 offset:9216
	ds_read_b128 v[110:113], v172 offset:9728
	v_cvt_pk_bf8_f32 v146, v82, v83
	v_cvt_pk_bf8_f32 v147, v86, v87
	v_exp_f32_e32 v69, v69
	v_exp_f32_e32 v70, v70
	v_exp_f32_e32 v71, v71
	s_waitcnt lgkmcnt(1)
	v_mfma_scale_f32_32x32x64_f8f6f4 v[114:129], v[98:105], v[138:145], v[2:17], v209, v208 op_sel_hi:[0,0,0]
	ds_read_b128 v[154:157], v172 offset:12288
	ds_read_b128 v[158:161], v172 offset:13312
	v_cvt_pk_bf8_f32 v146, v84, v85 op_sel:[0,0,1]
	v_cvt_pk_bf8_f32 v147, v88, v89 op_sel:[0,0,1]
	v_cvt_pk_bf8_f32 v148, v90, v91
	v_cvt_pk_bf8_f32 v149, v94, v95
	ds_read_b128 v[82:85], v172 offset:12800
	ds_read_b128 v[86:89], v172 offset:13824
	v_exp_f32_e32 v72, v72
	v_exp_f32_e32 v73, v73
	s_waitcnt lgkmcnt(4)
	v_mfma_scale_f32_32x32x64_f8f6f4 v[98:113], v[106:113], v[138:145], v[2:17], v209, v208 op_sel_hi:[0,0,0]
	v_cvt_pk_bf8_f32 v148, v92, v93 op_sel:[0,0,1]
	v_cvt_pk_bf8_f32 v149, v96, v97 op_sel:[0,0,1]
	ds_read_b128 v[90:93], v172 offset:16384
	ds_read_b128 v[94:97], v172 offset:17408
	v_exp_f32_e32 v74, v74
	v_exp_f32_e32 v75, v75
	v_exp_f32_e32 v76, v76
	s_waitcnt lgkmcnt(4)
	v_mfma_scale_f32_32x32x64_f8f6f4 v[114:129], v[154:161], v[130:137], v[114:129], v209, v208 op_sel_hi:[0,0,0]
	v_exp_f32_e32 v77, v77
	v_exp_f32_e32 v78, v78
	v_exp_f32_e32 v79, v79
	v_exp_f32_e32 v80, v80
	v_exp_f32_e32 v81, v81
	s_waitcnt lgkmcnt(2)
	v_mfma_scale_f32_32x32x64_f8f6f4 v[98:113], v[82:89], v[130:137], v[98:113], v209, v208 op_sel_hi:[0,0,0]
	v_cvt_pk_bf8_f32 v150, v66, v67
	v_cvt_pk_bf8_f32 v151, v70, v71
	v_cvt_pk_bf8_f32 v150, v68, v69 op_sel:[0,0,1]
	v_cvt_pk_bf8_f32 v151, v72, v73 op_sel:[0,0,1]
	v_cvt_pk_bf8_f32 v152, v74, v75
	v_cvt_pk_bf8_f32 v153, v78, v79
	v_cvt_pk_bf8_f32 v152, v76, v77 op_sel:[0,0,1]
	v_cvt_pk_bf8_f32 v153, v80, v81 op_sel:[0,0,1]
	ds_read_b128 v[66:69], v172 offset:16896
	ds_read_b128 v[70:73], v172 offset:17920
	s_waitcnt lgkmcnt(2)
	v_mfma_scale_f32_32x32x64_f8f6f4 v[50:65], v[90:97], v[146:153], v[50:65], v209, v209 op_sel_hi:[0,0,0] blgp:1
	s_nop 0
	v_exp_f32_e32 v114, v114
	v_exp_f32_e32 v115, v115
	v_exp_f32_e32 v116, v116
	v_exp_f32_e32 v117, v117
	v_exp_f32_e32 v118, v118
	v_exp_f32_e32 v119, v119
	v_add_u32_e32 v173, s3, v200
	ds_read_b128 v[74:77], v173 offset:512
	ds_read_b128 v[78:81], v173 offset:1536
	s_waitcnt lgkmcnt(2)
	v_mfma_scale_f32_32x32x64_f8f6f4 v[18:33], v[66:73], v[146:153], v[18:33], v209, v209 op_sel_hi:[0,0,0] blgp:1
	v_exp_f32_e32 v120, v120
	v_exp_f32_e32 v121, v121
	v_exp_f32_e32 v122, v122
	v_exp_f32_e32 v123, v123
	v_exp_f32_e32 v124, v124
	v_exp_f32_e32 v125, v125
	ds_read_b128 v[66:69], v173
	ds_read_b128 v[70:73], v173 offset:1024
	v_mfma_scale_f32_32x32x64_f8f6f4 v[34:49], v[210:217], v[146:153], v[34:49], v209, v209 op_sel_hi:[0,0,0] blgp:1
	v_exp_f32_e32 v126, v126
	v_exp_f32_e32 v127, v127
	v_exp_f32_e32 v128, v128
	v_exp_f32_e32 v129, v129
	v_exp_f32_e32 v98, v98
	v_exp_f32_e32 v99, v99
	v_exp_f32_e32 v100, v100
	s_add_i32 s61, s61, 1
	s_add_i32 s2, s62, 1
	s_and_b32 s62, s2, 3
	s_mul_i32 s64, s62, 0x6000
	s_add_i32 s2, s62, 2
	s_and_b32 s2, s2, 3
	s_mul_i32 s2, s2, 0x6000
	s_cmp_eq_u32 s62, 2
	s_cselect_b64 s[8:9], -1, 0
	s_cmp_eq_u32 s100, 0
	s_cbranch_scc1 .Lmla_w0
	s_cmp_eq_u32 s100, 1
	s_cbranch_scc1 .Lmla_w1
	s_waitcnt vmcnt(2)
	s_branch .Lmla_wd

; #define LAS __attribute__((address_space(3)))
; #define WAITV(n) asm volatile("s_waitcnt vmcnt(%0)" ::"n"(n) : "memory")
; DEV float ex2(float x) { return __builtin_amdgcn_exp2f(x); }
; #define MLA_SB() __builtin_amdgcn_sched_barrier(0)
; template <int VAR> DEV void mla_step(f32x16& C0, f32x16& C1, f32x16& P0, f32x16& P1, f32x16& o0, f32x16& o1, f32x16& lacc,
;                   const v8i (&qf)[2], const f32x16& cini, LAS char* kp, LAS char* vp, v8i& pw) {
;     v8i kf[2], vf[2];
;     const v8i ones8 = {0x38383838, 0x38383838, 0x38383838, 0x38383838, 0x38383838, 0x38383838, 0x38383838, 0x38383838};
;     kf[0] = mla_kf8(kp, 0, 0); kf[1] = mla_kf8(kp, 1, 0);
;     MLA_SB();
; #pragma unroll
;     for (int g = 0; g < 4; ++g) {
;         const int kb = g & 1, sx = g >> 1;
;         if (kb) C1 = MFMA8(kf[1], qf[sx], sx == 0 ? cini : C1); else C0 = MFMA8(kf[0], qf[sx], sx == 0 ? cini : C0);
;         if (g < 2) kf[kb] = mla_kf8(kp, kb, 1);
;         if (g >= 2) vf[g - 2] = mla_vf8(vp, g - 2);
; #pragma unroll
;         for (int j = 0; j < 2; ++j) { const int w = 2 * g + j, e = 4 * w;
;             if (VAR == 3) pw[w] = __builtin_bit_cast(int, (e < 16) ? P0[e] : P1[e - 16]);
;             else pw[w] = (int)((e < 16) ? pk_bf8x4(P0[e], P0[e + 1], P0[e + 2], P0[e + 3], pw[w]) : pk_bf8x4(P1[e - 16], P1[e - 15], P1[e - 14], P1[e - 13], pw[w])); }
;         if (g == 3) MLA_PIN(pw);
;         MLA_SB();
;     }
; #pragma unroll
;     for (int g = 0; g < 3; ++g) {
;         if (g == 0) o0 = MFMA8PV(vf[0], pw, o0); else if (g == 1) o1 = MFMA8PV(vf[1], pw, o1); else lacc = MFMA8PV(ones8, pw, lacc);
;         const int e0 = (g * 32) / 3, e1 = ((g + 1) * 32) / 3;
; #pragma unroll
;         for (int e = e0; e < e1; ++e) { if (VAR == 2 || VAR == 3) continue; if (e < 16) C0[e] = ex2(C0[e]); else C1[e - 16] = ex2(C1[e - 16]); }
;         if (g < 2) MLA_PIN(C0);
;         if (g > 0) MLA_PIN(C1);
;         MLA_SB();
;     }
; }
; template <int VAR> DEV void mla_unit(const Params& p, int layer, int b, int hd, int tokbase, int t0, int t1, LAS char* lds, SideJob& sj) {
;     ...
;             WAITV(0); SBAR();
;             if (s + 2 < ns) MLA_ISSUE(t0 + s + 2, (nslot == 2) ? 0 : nslot + 1);
;             { LAS char* nb = lds + nslot * STG; LAS char* ob = lds + slot * STG; mla_step<VAR>(sA0, sA1, sB0, sB1, o0, o1, lacc, qf, cini, nb + koffl, ob + MLA_VSUB + voffl, pw); }
.Lmla_wd:
	s_waitcnt lgkmcnt(0)
	s_barrier
	s_add_i32 s2, s2, s60
	s_mov_b32 s3, m0
	s_mov_b32 m0, s2
	v_cvt_pk_bf8_f32 v146, v114, v115
	v_cvt_pk_bf8_f32 v147, v118, v119
	v_exp_f32_e32 v101, v101
	v_exp_f32_e32 v102, v102
	v_exp_f32_e32 v103, v103
	s_waitcnt lgkmcnt(0)
	v_mfma_scale_f32_32x32x64_f8f6f4 v[82:97], v[66:73], v[138:145], v[2:17], v209, v208 op_sel_hi:[0,0,0]
	global_load_lds_dwordx4 v[162:163], off
	ds_read_b128 v[164:167], v173 offset:4096
	ds_read_b128 v[168:171], v173 offset:5120
	v_cvt_pk_bf8_f32 v146, v116, v117 op_sel:[0,0,1]
	v_cvt_pk_bf8_f32 v147, v120, v121 op_sel:[0,0,1]
	v_cvt_pk_bf8_f32 v148, v122, v123
	v_cvt_pk_bf8_f32 v149, v126, v127
	ds_read_b128 v[114:117], v173 offset:4608
	ds_read_b128 v[118:121], v173 offset:5632
	v_exp_f32_e32 v104, v104
	v_exp_f32_e32 v105, v105
	s_waitcnt lgkmcnt(4)
	v_mfma_scale_f32_32x32x64_f8f6f4 v[66:81], v[74:81], v[138:145], v[2:17], v209, v208 op_sel_hi:[0,0,0]
	global_load_lds_dwordx4 v[162:163], off offset:1024
	v_cvt_pk_bf8_f32 v148, v124, v125 op_sel:[0,0,1]
	v_cvt_pk_bf8_f32 v149, v128, v129 op_sel:[0,0,1]
	ds_read_b128 v[122:125], v172 offset:20480
	ds_read_b128 v[126:129], v172 offset:21504
	v_exp_f32_e32 v106, v106
	v_exp_f32_e32 v107, v107
	v_exp_f32_e32 v108, v108
	s_waitcnt lgkmcnt(4)
	v_mfma_scale_f32_32x32x64_f8f6f4 v[82:97], v[164:171], v[130:137], v[82:97], v209, v208 op_sel_hi:[0,0,0]
	global_load_lds_dwordx4 v[162:163], off offset:2048
	s_mov_b32 m0, s3
	v_exp_f32_e32 v109, v109
	v_exp_f32_e32 v110, v110
	v_exp_f32_e32 v111, v111
	v_exp_f32_e32 v112, v112
	v_exp_f32_e32 v113, v113
	s_waitcnt lgkmcnt(2)
	v_mfma_scale_f32_32x32x64_f8f6f4 v[66:81], v[114:121], v[130:137], v[66:81], v209, v208 op_sel_hi:[0,0,0]
	v_cvt_pk_bf8_f32 v150, v98, v99
	v_cvt_pk_bf8_f32 v151, v102, v103
	v_cvt_pk_bf8_f32 v150, v100, v101 op_sel:[0,0,1]
	v_cvt_pk_bf8_f32 v151, v104, v105 op_sel:[0,0,1]
	v_cvt_pk_bf8_f32 v152, v106, v107
	v_cvt_pk_bf8_f32 v153, v110, v111
	v_cvt_pk_bf8_f32 v152, v108, v109 op_sel:[0,0,1]
	v_cvt_pk_bf8_f32 v153, v112, v113 op_sel:[0,0,1]
	ds_read_b128 v[98:101], v172 offset:20992
	ds_read_b128 v[102:105], v172 offset:22016
	s_waitcnt lgkmcnt(2)
	v_mfma_scale_f32_32x32x64_f8f6f4 v[50:65], v[122:129], v[146:153], v[50:65], v209, v209 op_sel_hi:[0,0,0] blgp:1
	s_nop 0
	v_exp_f32_e32 v82, v82
	v_exp_f32_e32 v83, v83
	v_exp_f32_e32 v84, v84
	v_exp_f32_e32 v85, v85
	v_exp_f32_e32 v86, v86
	v_exp_f32_e32 v87, v87
	s_waitcnt lgkmcnt(0)
	v_mfma_scale_f32_32x32x64_f8f6f4 v[18:33], v[98:105], v[146:153], v[18:33], v209, v209 op_sel_hi:[0,0,0] blgp:1
	v_exp_f32_e32 v88, v88
	v_exp_f32_e32 v89, v89
	v_exp_f32_e32 v90, v90
	v_exp_f32_e32 v91, v91
	v_exp_f32_e32 v92, v92
	v_exp_f32_e32 v93, v93
	v_mfma_scale_f32_32x32x64_f8f6f4 v[34:49], v[210:217], v[146:153], v[34:49], v209, v209 op_sel_hi:[0,0,0] blgp:1
	v_exp_f32_e32 v94, v94
	v_exp_f32_e32 v95, v95
	v_exp_f32_e32 v96, v96
	v_exp_f32_e32 v97, v97
	v_exp_f32_e32 v66, v66
	v_exp_f32_e32 v67, v67
	v_exp_f32_e32 v68, v68
	s_mov_b64 s[20:21], 0x6000
	s_cmpk_lg_i32 s61, 0x80
	v_lshl_add_u64 v[162:163], v[162:163], 0, s[20:21]
	s_cbranch_scc0 .LBB0_835
